# speedup vs baseline: 1.0442x; 1.0014x over previous
.LBB1_82:
	ds_read_b128 v[130:133], v219 offset:32768
	ds_read_b128 v[134:137], v219 offset:33792
	ds_read_b128 v[138:141], v219 offset:34816
	ds_read_b128 v[142:145], v219 offset:35840
	ds_read_b128 v[178:181], v219 offset:49152
	ds_read_b128 v[182:185], v219 offset:50176
	ds_read_b128 v[186:189], v219 offset:51200
	ds_read_b128 v[190:193], v219 offset:52224
	ds_read_b128 v[146:149], v220
	ds_read_b128 v[150:153], v220 offset:1024
	ds_read_b128 v[154:157], v221
	ds_read_b128 v[158:161], v221 offset:1024
	ds_read_b128 v[162:165], v222
	ds_read_b128 v[166:169], v222 offset:1024
	ds_read_b128 v[170:173], v223
	ds_read_b128 v[174:177], v223 offset:1024
	s_add_i32 s12, s8, 1
	v_readlane_b32 s9, v248, s12
	s_mov_b32 m0, s43
	s_nop 1
	v_add_u32_e32 v251, s9, v249
	global_load_lds_dwordx4 v251, s[18:19]
	v_add_u32_e32 v251, s9, v250
	s_mov_b32 m0, s44
	s_nop 0
	global_load_lds_dwordx4 v251, s[18:19]
	s_waitcnt vmcnt(8) lgkmcnt(0)
	s_barrier
	s_setprio 1
	v_mfma_f32_16x16x32_f16 v[124:127], v[130:133], v[146:149], v[124:127]
	v_mfma_f32_16x16x32_f16 v[120:123], v[138:141], v[146:149], v[120:123]
	v_mfma_f32_16x16x32_f16 v[116:119], v[130:133], v[154:157], v[116:119]
	v_mfma_f32_16x16x32_f16 v[112:115], v[138:141], v[154:157], v[112:115]
	v_mfma_f32_16x16x32_f16 v[108:111], v[130:133], v[162:165], v[108:111]
	v_mfma_f32_16x16x32_f16 v[104:107], v[138:141], v[162:165], v[104:107]
	v_mfma_f32_16x16x32_f16 v[100:103], v[130:133], v[170:173], v[100:103]
	v_mfma_f32_16x16x32_f16 v[96:99], v[138:141], v[170:173], v[96:99]
	v_mfma_f32_16x16x32_f16 v[124:127], v[134:137], v[150:153], v[124:127]
	v_mfma_f32_16x16x32_f16 v[120:123], v[142:145], v[150:153], v[120:123]
	v_mfma_f32_16x16x32_f16 v[116:119], v[134:137], v[158:161], v[116:119]
	v_mfma_f32_16x16x32_f16 v[112:115], v[142:145], v[158:161], v[112:115]
	v_mfma_f32_16x16x32_f16 v[108:111], v[134:137], v[166:169], v[108:111]
	v_mfma_f32_16x16x32_f16 v[104:107], v[142:145], v[166:169], v[104:107]
	v_mfma_f32_16x16x32_f16 v[100:103], v[134:137], v[174:177], v[100:103]
	v_mfma_f32_16x16x32_f16 v[96:99], v[142:145], v[174:177], v[96:99]
	v_mfma_f32_16x16x32_f16 v[52:55], v[178:181], v[146:149], v[52:55]
	v_mfma_f32_16x16x32_f16 v[40:43], v[186:189], v[146:149], v[40:43]
	v_mfma_f32_16x16x32_f16 v[36:39], v[178:181], v[154:157], v[36:39]
	v_mfma_f32_16x16x32_f16 v[32:35], v[186:189], v[154:157], v[32:35]
	v_mfma_f32_16x16x32_f16 v[28:31], v[178:181], v[162:165], v[28:31]
	v_mfma_f32_16x16x32_f16 v[24:27], v[186:189], v[162:165], v[24:27]
	v_mfma_f32_16x16x32_f16 v[20:23], v[178:181], v[170:173], v[20:23]
	v_mfma_f32_16x16x32_f16 v[16:19], v[186:189], v[170:173], v[16:19]
	v_mfma_f32_16x16x32_f16 v[52:55], v[182:185], v[150:153], v[52:55]
	v_mfma_f32_16x16x32_f16 v[40:43], v[190:193], v[150:153], v[40:43]
	v_mfma_f32_16x16x32_f16 v[36:39], v[182:185], v[158:161], v[36:39]
	v_mfma_f32_16x16x32_f16 v[32:35], v[190:193], v[158:161], v[32:35]
	v_mfma_f32_16x16x32_f16 v[28:31], v[182:185], v[166:169], v[28:31]
	v_mfma_f32_16x16x32_f16 v[24:27], v[190:193], v[166:169], v[24:27]
	v_mfma_f32_16x16x32_f16 v[20:23], v[182:185], v[174:177], v[20:23]
	v_mfma_f32_16x16x32_f16 v[16:19], v[190:193], v[174:177], v[16:19]
	s_setprio 0
	s_barrier
	ds_read_b128 v[146:149], v220 offset:16384
	ds_read_b128 v[150:153], v220 offset:17408
	ds_read_b128 v[154:157], v221 offset:16384
	ds_read_b128 v[158:161], v221 offset:17408
	ds_read_b128 v[162:165], v222 offset:16384
	ds_read_b128 v[166:169], v222 offset:17408
	ds_read_b128 v[170:173], v223 offset:16384
	ds_read_b128 v[174:177], v223 offset:17408
	v_add_u32_e32 v129, s7, v128
	s_mov_b32 m0, s22
	v_add_u32_e32 v194, 0xffffff80, v129
	global_load_lds_dwordx4 v194, s[10:11]
	v_add_u32_e32 v194, 0x47f80, v129
	s_mov_b32 m0, s23
	s_add_i32 s9, s8, 2
	global_load_lds_dwordx4 v194, s[10:11]
	v_readlane_b32 s13, v248, s9
	s_mov_b32 m0, s21
	s_nop 1
	v_add_u32_e32 v194, s13, v206
	global_load_lds_dwordx4 v194, s[18:19]
	v_add_u32_e32 v194, s13, v213
	s_mov_b32 m0, s24
	s_nop 0
	global_load_lds_dwordx4 v194, s[18:19]
	s_mov_b32 m0, s25
	v_add_u32_e32 v194, 0x8ff80, v129
	global_load_lds_dwordx4 v194, s[10:11]
	v_add_u32_e32 v194, 0xd7f80, v129
	s_mov_b32 m0, s26
	s_nop 0
	global_load_lds_dwordx4 v194, s[10:11]
	s_waitcnt vmcnt(8) lgkmcnt(0)
	s_barrier
	s_setprio 1
	v_mfma_f32_16x16x32_f16 v[12:15], v[130:133], v[146:149], v[12:15]
	v_mfma_f32_16x16x32_f16 v[8:11], v[138:141], v[146:149], v[8:11]
	v_mfma_f32_16x16x32_f16 v[4:7], v[130:133], v[154:157], v[4:7]
	v_mfma_f32_16x16x32_f16 v[0:3], v[138:141], v[154:157], v[0:3]
	v_mfma_f32_16x16x32_f16 v[44:47], v[130:133], v[162:165], v[44:47]
	v_mfma_f32_16x16x32_f16 v[48:51], v[138:141], v[162:165], v[48:51]
	v_mfma_f32_16x16x32_f16 v[56:59], v[130:133], v[170:173], v[56:59]
	v_mfma_f32_16x16x32_f16 v[60:63], v[138:141], v[170:173], v[60:63]
	v_mfma_f32_16x16x32_f16 v[12:15], v[134:137], v[150:153], v[12:15]
	v_mfma_f32_16x16x32_f16 v[8:11], v[142:145], v[150:153], v[8:11]
	v_mfma_f32_16x16x32_f16 v[4:7], v[134:137], v[158:161], v[4:7]
	v_mfma_f32_16x16x32_f16 v[0:3], v[142:145], v[158:161], v[0:3]
	v_mfma_f32_16x16x32_f16 v[44:47], v[134:137], v[166:169], v[44:47]
	v_mfma_f32_16x16x32_f16 v[48:51], v[142:145], v[166:169], v[48:51]
	v_mfma_f32_16x16x32_f16 v[56:59], v[134:137], v[174:177], v[56:59]
	v_mfma_f32_16x16x32_f16 v[60:63], v[142:145], v[174:177], v[60:63]
	v_mfma_f32_16x16x32_f16 v[64:67], v[178:181], v[146:149], v[64:67]
	v_mfma_f32_16x16x32_f16 v[68:71], v[186:189], v[146:149], v[68:71]
	v_mfma_f32_16x16x32_f16 v[72:75], v[178:181], v[154:157], v[72:75]
	v_mfma_f32_16x16x32_f16 v[76:79], v[186:189], v[154:157], v[76:79]
	v_mfma_f32_16x16x32_f16 v[80:83], v[178:181], v[162:165], v[80:83]
	v_mfma_f32_16x16x32_f16 v[84:87], v[186:189], v[162:165], v[84:87]
	v_mfma_f32_16x16x32_f16 v[88:91], v[178:181], v[170:173], v[88:91]
	v_mfma_f32_16x16x32_f16 v[92:95], v[186:189], v[170:173], v[92:95]
	v_mfma_f32_16x16x32_f16 v[64:67], v[182:185], v[150:153], v[64:67]
	v_mfma_f32_16x16x32_f16 v[68:71], v[190:193], v[150:153], v[68:71]
	v_mfma_f32_16x16x32_f16 v[72:75], v[182:185], v[158:161], v[72:75]
	v_mfma_f32_16x16x32_f16 v[76:79], v[190:193], v[158:161], v[76:79]
	v_mfma_f32_16x16x32_f16 v[80:83], v[182:185], v[166:169], v[80:83]
	v_mfma_f32_16x16x32_f16 v[84:87], v[190:193], v[166:169], v[84:87]
	v_mfma_f32_16x16x32_f16 v[88:91], v[182:185], v[174:177], v[88:91]
	v_mfma_f32_16x16x32_f16 v[92:95], v[190:193], v[174:177], v[92:95]
	s_setprio 0
	s_barrier
	ds_read_b128 v[130:133], v224
	ds_read_b128 v[134:137], v224 offset:1024
	ds_read_b128 v[138:141], v224 offset:2048
	ds_read_b128 v[142:145], v224 offset:3072
	ds_read_b128 v[178:181], v229
	ds_read_b128 v[182:185], v229 offset:1024
	ds_read_b128 v[186:189], v229 offset:2048
	ds_read_b128 v[190:193], v229 offset:3072
	ds_read_b128 v[146:149], v225
	ds_read_b128 v[150:153], v225 offset:1024
	ds_read_b128 v[154:157], v226
	ds_read_b128 v[158:161], v226 offset:1024
	ds_read_b128 v[162:165], v227
	ds_read_b128 v[166:169], v227 offset:1024
	ds_read_b128 v[170:173], v228
	ds_read_b128 v[174:177], v228 offset:1024
	v_readlane_b32 s12, v248, s9
	s_mov_b32 m0, s27
	s_nop 1
	v_add_u32_e32 v251, s12, v249
	global_load_lds_dwordx4 v251, s[18:19]
	v_add_u32_e32 v251, s12, v250
	s_mov_b32 m0, s28
	s_nop 0
	global_load_lds_dwordx4 v251, s[18:19]
	s_waitcnt vmcnt(8) lgkmcnt(0)
	s_barrier
	s_setprio 1
	v_mfma_f32_16x16x32_f16 v[124:127], v[130:133], v[146:149], v[124:127]
	v_mfma_f32_16x16x32_f16 v[120:123], v[138:141], v[146:149], v[120:123]
	v_mfma_f32_16x16x32_f16 v[116:119], v[130:133], v[154:157], v[116:119]
	v_mfma_f32_16x16x32_f16 v[112:115], v[138:141], v[154:157], v[112:115]
	v_mfma_f32_16x16x32_f16 v[108:111], v[130:133], v[162:165], v[108:111]
	v_mfma_f32_16x16x32_f16 v[104:107], v[138:141], v[162:165], v[104:107]
	v_mfma_f32_16x16x32_f16 v[100:103], v[130:133], v[170:173], v[100:103]
	v_mfma_f32_16x16x32_f16 v[96:99], v[138:141], v[170:173], v[96:99]
	v_mfma_f32_16x16x32_f16 v[124:127], v[134:137], v[150:153], v[124:127]
	v_mfma_f32_16x16x32_f16 v[120:123], v[142:145], v[150:153], v[120:123]
	v_mfma_f32_16x16x32_f16 v[116:119], v[134:137], v[158:161], v[116:119]
	v_mfma_f32_16x16x32_f16 v[112:115], v[142:145], v[158:161], v[112:115]
	v_mfma_f32_16x16x32_f16 v[108:111], v[134:137], v[166:169], v[108:111]
	v_mfma_f32_16x16x32_f16 v[104:107], v[142:145], v[166:169], v[104:107]
	v_mfma_f32_16x16x32_f16 v[100:103], v[134:137], v[174:177], v[100:103]
	v_mfma_f32_16x16x32_f16 v[96:99], v[142:145], v[174:177], v[96:99]
	v_mfma_f32_16x16x32_f16 v[52:55], v[178:181], v[146:149], v[52:55]
	v_mfma_f32_16x16x32_f16 v[40:43], v[186:189], v[146:149], v[40:43]
	v_mfma_f32_16x16x32_f16 v[36:39], v[178:181], v[154:157], v[36:39]
	v_mfma_f32_16x16x32_f16 v[32:35], v[186:189], v[154:157], v[32:35]
	v_mfma_f32_16x16x32_f16 v[28:31], v[178:181], v[162:165], v[28:31]
	v_mfma_f32_16x16x32_f16 v[24:27], v[186:189], v[162:165], v[24:27]
	v_mfma_f32_16x16x32_f16 v[20:23], v[178:181], v[170:173], v[20:23]
	v_mfma_f32_16x16x32_f16 v[16:19], v[186:189], v[170:173], v[16:19]
	v_mfma_f32_16x16x32_f16 v[52:55], v[182:185], v[150:153], v[52:55]
	v_mfma_f32_16x16x32_f16 v[40:43], v[190:193], v[150:153], v[40:43]
	v_mfma_f32_16x16x32_f16 v[36:39], v[182:185], v[158:161], v[36:39]
	v_mfma_f32_16x16x32_f16 v[32:35], v[190:193], v[158:161], v[32:35]
	v_mfma_f32_16x16x32_f16 v[28:31], v[182:185], v[166:169], v[28:31]
	v_mfma_f32_16x16x32_f16 v[24:27], v[190:193], v[166:169], v[24:27]
	v_mfma_f32_16x16x32_f16 v[20:23], v[182:185], v[174:177], v[20:23]
	v_mfma_f32_16x16x32_f16 v[16:19], v[190:193], v[174:177], v[16:19]
	s_setprio 0
	s_barrier
	ds_read_b128 v[146:149], v230
	ds_read_b128 v[150:153], v230 offset:1024
	ds_read_b128 v[154:157], v231
	ds_read_b128 v[158:161], v231 offset:1024
	ds_read_b128 v[162:165], v232
	ds_read_b128 v[166:169], v232 offset:1024
	ds_read_b128 v[170:173], v233
	ds_read_b128 v[174:177], v233 offset:1024
	s_mov_b32 m0, s37
	v_add_u32_e32 v194, 0x48000, v129
	global_load_lds_dwordx4 v129, s[10:11]
	s_mov_b32 m0, s38
	s_add_i32 s12, s8, 3
	global_load_lds_dwordx4 v194, s[10:11]
	v_readlane_b32 s13, v248, s12
	s_mov_b32 m0, s39
	s_nop 1
	v_add_u32_e32 v194, s13, v206
	global_load_lds_dwordx4 v194, s[18:19]
	v_add_u32_e32 v194, s13, v213
	s_mov_b32 m0, s40
	s_nop 0
	global_load_lds_dwordx4 v194, s[18:19]
	s_mov_b32 m0, s41
	v_add_u32_e32 v194, 0x90000, v129
	global_load_lds_dwordx4 v194, s[10:11]
	v_add_u32_e32 v194, 0xd8000, v129
	s_mov_b32 m0, s42
	s_nop 0
	global_load_lds_dwordx4 v194, s[10:11]
	s_waitcnt vmcnt(8) lgkmcnt(0)
	s_barrier
	s_setprio 1
	v_mfma_f32_16x16x32_f16 v[12:15], v[130:133], v[146:149], v[12:15]
	v_mfma_f32_16x16x32_f16 v[8:11], v[138:141], v[146:149], v[8:11]
	v_mfma_f32_16x16x32_f16 v[4:7], v[130:133], v[154:157], v[4:7]
	v_mfma_f32_16x16x32_f16 v[0:3], v[138:141], v[154:157], v[0:3]
	v_mfma_f32_16x16x32_f16 v[44:47], v[130:133], v[162:165], v[44:47]
	v_mfma_f32_16x16x32_f16 v[48:51], v[138:141], v[162:165], v[48:51]
	v_mfma_f32_16x16x32_f16 v[56:59], v[130:133], v[170:173], v[56:59]
	v_mfma_f32_16x16x32_f16 v[60:63], v[138:141], v[170:173], v[60:63]
	v_mfma_f32_16x16x32_f16 v[12:15], v[134:137], v[150:153], v[12:15]
	v_mfma_f32_16x16x32_f16 v[8:11], v[142:145], v[150:153], v[8:11]
	v_mfma_f32_16x16x32_f16 v[4:7], v[134:137], v[158:161], v[4:7]
	v_mfma_f32_16x16x32_f16 v[0:3], v[142:145], v[158:161], v[0:3]
	v_mfma_f32_16x16x32_f16 v[44:47], v[134:137], v[166:169], v[44:47]
	v_mfma_f32_16x16x32_f16 v[48:51], v[142:145], v[166:169], v[48:51]
	v_mfma_f32_16x16x32_f16 v[56:59], v[134:137], v[174:177], v[56:59]
	v_mfma_f32_16x16x32_f16 v[60:63], v[142:145], v[174:177], v[60:63]
	v_mfma_f32_16x16x32_f16 v[64:67], v[178:181], v[146:149], v[64:67]
	v_mfma_f32_16x16x32_f16 v[68:71], v[186:189], v[146:149], v[68:71]
	v_mfma_f32_16x16x32_f16 v[72:75], v[178:181], v[154:157], v[72:75]
	v_mfma_f32_16x16x32_f16 v[76:79], v[186:189], v[154:157], v[76:79]
	v_mfma_f32_16x16x32_f16 v[80:83], v[178:181], v[162:165], v[80:83]
	v_mfma_f32_16x16x32_f16 v[84:87], v[186:189], v[162:165], v[84:87]
	v_mfma_f32_16x16x32_f16 v[88:91], v[178:181], v[170:173], v[88:91]
	v_mfma_f32_16x16x32_f16 v[92:95], v[186:189], v[170:173], v[92:95]
	v_mfma_f32_16x16x32_f16 v[64:67], v[182:185], v[150:153], v[64:67]
	v_mfma_f32_16x16x32_f16 v[68:71], v[190:193], v[150:153], v[68:71]
	v_mfma_f32_16x16x32_f16 v[72:75], v[182:185], v[158:161], v[72:75]
	v_mfma_f32_16x16x32_f16 v[76:79], v[190:193], v[158:161], v[76:79]
	v_mfma_f32_16x16x32_f16 v[80:83], v[182:185], v[166:169], v[80:83]
	v_mfma_f32_16x16x32_f16 v[84:87], v[190:193], v[166:169], v[84:87]
	v_mfma_f32_16x16x32_f16 v[88:91], v[182:185], v[174:177], v[88:91]
	v_mfma_f32_16x16x32_f16 v[92:95], v[190:193], v[174:177], v[92:95]
	s_setprio 0
	s_addk_i32 s7, 0x100
	s_cmp_lt_u32 s8, 32
	s_mov_b32 s8, s9
	s_barrier
	s_cbranch_scc1 .LBB1_82
	ds_read_b128 v[132:135], v219 offset:32768
	ds_read_b128 v[136:139], v219 offset:33792
	ds_read_b128 v[140:143], v219 offset:34816
	ds_read_b128 v[144:147], v219 offset:35840
	ds_read_b128 v[128:131], v220
	ds_read_b128 v[148:151], v220 offset:1024
	ds_read_b128 v[152:155], v221
	ds_read_b128 v[156:159], v221 offset:1024
	ds_read_b128 v[188:191], v222
	ds_read_b128 v[192:195], v222 offset:1024
	ds_read_b128 v[196:199], v223
	ds_read_b128 v[200:203], v223 offset:1024
	s_setprio 2
	s_lshl_b32 s3, s50, 9
	s_add_i32 s3, s47, s3
	s_add_i32 s3, s3, 0x10380
	s_mov_b32 m0, s43
	v_add_u32_e32 v160, s3, v206
	global_load_lds_dwordx4 v160, s[18:19]
	v_add_u32_e32 v160, s3, v213
	s_mov_b32 m0, s44
	s_nop 0
	global_load_lds_dwordx4 v160, s[18:19]
	s_setprio 0
	s_waitcnt vmcnt(8)
	s_barrier
	s_waitcnt lgkmcnt(0)
	s_setprio 1
	s_waitcnt lgkmcnt(0)
	v_mfma_f32_16x16x32_f16 v[124:127], v[132:135], v[128:131], v[124:127]
	v_mfma_f32_16x16x32_f16 v[120:123], v[140:143], v[128:131], v[120:123]
	v_mfma_f32_16x16x32_f16 v[116:119], v[132:135], v[152:155], v[116:119]
	v_mfma_f32_16x16x32_f16 v[112:115], v[140:143], v[152:155], v[112:115]
	v_mfma_f32_16x16x32_f16 v[108:111], v[132:135], v[188:191], v[108:111]
	v_mfma_f32_16x16x32_f16 v[104:107], v[140:143], v[188:191], v[104:107]
	v_mfma_f32_16x16x32_f16 v[100:103], v[132:135], v[196:199], v[100:103]
	v_mfma_f32_16x16x32_f16 v[96:99], v[140:143], v[196:199], v[96:99]
	v_mfma_f32_16x16x32_f16 v[160:163], v[136:139], v[148:151], v[124:127]
	v_mfma_f32_16x16x32_f16 v[164:167], v[144:147], v[148:151], v[120:123]
	v_mfma_f32_16x16x32_f16 v[168:171], v[136:139], v[156:159], v[116:119]
	v_mfma_f32_16x16x32_f16 v[172:175], v[144:147], v[156:159], v[112:115]
	v_mfma_f32_16x16x32_f16 v[176:179], v[136:139], v[192:195], v[108:111]
	v_mfma_f32_16x16x32_f16 v[180:183], v[144:147], v[192:195], v[104:107]
	v_mfma_f32_16x16x32_f16 v[100:103], v[136:139], v[200:203], v[100:103]
	v_mfma_f32_16x16x32_f16 v[184:187], v[144:147], v[200:203], v[96:99]
	s_setprio 0
	s_barrier
	ds_read_b128 v[104:107], v219 offset:49152
	ds_read_b128 v[108:111], v219 offset:50176
	ds_read_b128 v[116:119], v219 offset:51200
	ds_read_b128 v[236:239], v219 offset:52224
	s_barrier
	s_waitcnt lgkmcnt(0)
	s_setprio 1
	s_waitcnt lgkmcnt(0)
	v_mfma_f32_16x16x32_f16 v[52:55], v[104:107], v[128:131], v[52:55]
	v_mfma_f32_16x16x32_f16 v[40:43], v[116:119], v[128:131], v[40:43]
	v_mfma_f32_16x16x32_f16 v[36:39], v[104:107], v[152:155], v[36:39]
	v_mfma_f32_16x16x32_f16 v[32:35], v[116:119], v[152:155], v[32:35]
	v_mfma_f32_16x16x32_f16 v[28:31], v[104:107], v[188:191], v[28:31]
	v_mfma_f32_16x16x32_f16 v[24:27], v[116:119], v[188:191], v[24:27]
	v_mfma_f32_16x16x32_f16 v[20:23], v[104:107], v[196:199], v[20:23]
	v_mfma_f32_16x16x32_f16 v[16:19], v[116:119], v[196:199], v[16:19]
	v_mfma_f32_16x16x32_f16 v[52:55], v[108:111], v[148:151], v[52:55]
	v_mfma_f32_16x16x32_f16 v[40:43], v[236:239], v[148:151], v[40:43]
	v_mfma_f32_16x16x32_f16 v[36:39], v[108:111], v[156:159], v[36:39]
	v_mfma_f32_16x16x32_f16 v[32:35], v[236:239], v[156:159], v[32:35]
	v_mfma_f32_16x16x32_f16 v[28:31], v[108:111], v[192:195], v[28:31]
	v_mfma_f32_16x16x32_f16 v[24:27], v[236:239], v[192:195], v[24:27]
	v_mfma_f32_16x16x32_f16 v[96:99], v[108:111], v[200:203], v[20:23]
	v_mfma_f32_16x16x32_f16 v[16:19], v[236:239], v[200:203], v[16:19]
	s_setprio 0
	s_barrier
	ds_read_b128 v[20:23], v220 offset:16384
	ds_read_b128 v[148:151], v220 offset:17408
	ds_read_b128 v[152:155], v221 offset:16384
	ds_read_b128 v[156:159], v221 offset:17408
	ds_read_b128 v[188:191], v222 offset:16384
	ds_read_b128 v[192:195], v222 offset:17408
	ds_read_b128 v[196:199], v223 offset:16384
	ds_read_b128 v[200:203], v223 offset:17408
	s_waitcnt vmcnt(4)
	s_barrier
	s_waitcnt lgkmcnt(0)
	s_setprio 1
	s_waitcnt lgkmcnt(0)
	v_mfma_f32_16x16x32_f16 v[0:3], v[140:143], v[152:155], v[0:3]
	v_mfma_f32_16x16x32_f16 v[124:127], v[144:147], v[156:159], v[0:3]
	v_mfma_f32_16x16x32_f16 v[0:3], v[132:135], v[188:191], v[44:47]
	v_mfma_f32_16x16x32_f16 v[128:131], v[136:139], v[192:195], v[0:3]
	v_mfma_f32_16x16x32_f16 v[0:3], v[140:143], v[188:191], v[48:51]
	v_mfma_f32_16x16x32_f16 v[48:51], v[144:147], v[192:195], v[0:3]
	v_mfma_f32_16x16x32_f16 v[0:3], v[132:135], v[196:199], v[56:59]
	v_mfma_f32_16x16x32_f16 v[12:15], v[132:135], v[20:23], v[12:15]
	v_mfma_f32_16x16x32_f16 v[8:11], v[140:143], v[20:23], v[8:11]
	v_mfma_f32_16x16x32_f16 v[4:7], v[132:135], v[152:155], v[4:7]
	v_mfma_f32_16x16x32_f16 v[56:59], v[136:139], v[200:203], v[0:3]
	v_mfma_f32_16x16x32_f16 v[0:3], v[140:143], v[196:199], v[60:63]
	v_mfma_f32_16x16x32_f16 v[112:115], v[136:139], v[148:151], v[12:15]
	v_mfma_f32_16x16x32_f16 v[8:11], v[144:147], v[148:151], v[8:11]
	v_mfma_f32_16x16x32_f16 v[120:123], v[136:139], v[156:159], v[4:7]
	v_mfma_f32_16x16x32_f16 v[60:63], v[144:147], v[200:203], v[0:3]
	s_setprio 0
	s_setprio 1
	v_mfma_f32_16x16x32_f16 v[0:3], v[104:107], v[20:23], v[64:67]
	v_mfma_f32_16x16x32_f16 v[132:135], v[108:111], v[148:151], v[0:3]
	v_mfma_f32_16x16x32_f16 v[0:3], v[116:119], v[20:23], v[68:71]
	v_mfma_f32_16x16x32_f16 v[136:139], v[236:239], v[148:151], v[0:3]
	v_mfma_f32_16x16x32_f16 v[0:3], v[104:107], v[152:155], v[72:75]
	v_mfma_f32_16x16x32_f16 v[140:143], v[108:111], v[156:159], v[0:3]
	v_mfma_f32_16x16x32_f16 v[0:3], v[116:119], v[152:155], v[76:79]
	v_mfma_f32_16x16x32_f16 v[144:147], v[236:239], v[156:159], v[0:3]
	v_mfma_f32_16x16x32_f16 v[0:3], v[104:107], v[188:191], v[80:83]
	v_mfma_f32_16x16x32_f16 v[80:83], v[108:111], v[192:195], v[0:3]
	v_mfma_f32_16x16x32_f16 v[0:3], v[116:119], v[188:191], v[84:87]
	v_mfma_f32_16x16x32_f16 v[148:151], v[236:239], v[192:195], v[0:3]
	v_mfma_f32_16x16x32_f16 v[0:3], v[104:107], v[196:199], v[88:91]
	v_mfma_f32_16x16x32_f16 v[152:155], v[108:111], v[200:203], v[0:3]
	v_mfma_f32_16x16x32_f16 v[0:3], v[116:119], v[196:199], v[92:95]
	v_mfma_f32_16x16x32_f16 v[156:159], v[236:239], v[200:203], v[0:3]
	s_setprio 0
	s_add_i32 s49, s49, s17
	s_cmpk_lt_i32 s49, 0x1c8
	s_cselect_b64 s[6:7], -1, 0
	s_cmpk_gt_i32 s49, 0x1c7
	s_cselect_b64 s[12:13], -1, 0
	s_and_b64 vcc, exec, s[12:13]
	s_mov_b32 s54, s2
	s_mov_b32 s53, s51
	s_mov_b32 s55, s52
	s_barrier
	s_cbranch_vccnz .LBB1_100
	s_cmpk_lt_i32 s49, 0x148
	s_cbranch_scc1 .LBB1_88
	s_cmpk_lt_u32 s49, 0x1a0
	s_cbranch_scc1 .LBB1_89
	s_cmpk_lt_u32 s49, 0x1b8
	s_cbranch_scc1 .LBB1_90
	s_cmpk_lt_u32 s49, 0x1c0
	s_cselect_b32 s47, s45, 0xfffffe40
	s_cselect_b32 s48, 3, 4
	s_mov_b32 s3, 1
	s_cmp_lt_i32 s48, 1
	s_movk_i32 s53, 0x64
	s_cbranch_scc0 .LBB1_91
	s_branch .LBB1_99

_Z10head_fusedPKDF16_S0_S0_PKfS2_S2_S2_S2_S2_S2_S2_Pf:
	s_mulk_i32 s3, 0x1c8
	s_add_i32 s3, s3, s2
	s_and_b32 s2, s2, 7
	s_ashr_i32 s37, s3, 3
	s_and_b32 s3, s37, 1
	s_mulk_i32 s3, 0x1c8
	s_lshr_b32 s37, s37, 1
	s_cmp_lt_u32 s37, 56
	s_cbranch_scc0 .Lhm_last
	s_lshr_b32 s4, s37, 3
	s_lshl_b32 s4, s4, 6
	s_and_b32 s37, s37, 7
	s_lshl_b32 s2, s2, 3
	s_add_i32 s37, s37, s2
	s_add_i32 s37, s37, s4
	s_branch .Lhm_done
.Lhm_last:
	s_add_i32 s37, s2, 0x1c0
.Lhm_done:
	s_add_i32 s37, s37, s3
	s_load_dwordx8 s[20:27], s[0:1], 0x40
	s_load_dwordx4 s[28:31], s[0:1], 0x0
	s_load_dwordx2 s[10:11], s[0:1], 0x10
	s_load_dwordx8 s[12:19], s[0:1], 0x20
	s_mul_hi_i32 s2, s37, 0x8fb823ef
	s_add_i32 s2, s2, s37
	s_lshr_b32 s3, s2, 31
	s_ashr_i32 s35, s2, 8
	s_add_i32 s35, s35, s3
	s_mul_i32 s2, s35, 0xfffffe38
	s_add_i32 s40, s2, s37
	s_mov_b32 s2, 41
	s_mov_b32 s34, 0
	s_cmpk_lt_i32 s40, 0x148
	s_mov_b32 s3, 0
	s_cbranch_scc1 .LBB2_6
	s_cmpk_lt_u32 s40, 0x1a0
	s_cbranch_scc1 .LBB2_4
	s_cmpk_lt_u32 s40, 0x1b8
	s_cbranch_scc1 .LBB2_5
	s_cmpk_lt_u32 s40, 0x1c0
	s_movk_i32 s2, 0xfe48
	s_cselect_b32 s3, s2, 0xfffffe40
	s_cselect_b32 s34, 3, 4
	s_mov_b32 s2, 1
	s_branch .LBB2_6
